# grid barrier: the last XCD leader releases every XCD's generation word directly, so other leaders and local workgroups poll one word and skip the cross-XCD generation hop
# speedup vs baseline: 1.0155x; 1.0083x over previous
; __device__ __forceinline__ unsigned xb_ld(unsigned* p)              { return __hip_atomic_load(p, __ATOMIC_RELAXED, __HIP_MEMORY_SCOPE_AGENT); }
; __device__ __forceinline__ unsigned xb_add(unsigned* p, unsigned v) { return __hip_atomic_fetch_add(p, v, __ATOMIC_RELAXED, __HIP_MEMORY_SCOPE_AGENT); }
; #define XB_SPIN(cond, bar) do { unsigned _sp = 0; while (cond) { __builtin_amdgcn_s_sleep(1); \
;     if ((++_sp & 255u) == 0u) { if (xb_ld(&(bar)[XB_TMO])) break; if (_sp > XB_SPIN_CAP) { atomicAdd(&(bar)[XB_TMO], 1u); break; } } } } while (0)
; __device__ __forceinline__ void xcd_barrier(const XcdBarrier& b) {
;     ...
;         const unsigned old = xb_add(&bar[XB_XSUB(b.x)], 1u);
;         const unsigned gen = old / nloc;
;         if (old + 1u == (gen + 1u) * nloc) {
;             asm volatile("buffer_inv sc1" ::: "memory");
;             __builtin_amdgcn_fence(__ATOMIC_RELEASE, "agent");
;             asm volatile("s_waitcnt vmcnt(0)" ::: "memory");
;             const unsigned og = xb_add(&bar[XB_TOP], 1u);
;             const unsigned tg = og / nx;
;             if (og + 1u == (tg + 1u) * nx) xb_add(&bar[XB_TOPGEN], 1u);
;             else XB_SPIN(xb_ld(&bar[XB_TOPGEN]) == tg, bar);
;             asm volatile("" ::: "memory");
;             xb_add(&bar[XB_XGEN(b.x)], 1u);
;             asm volatile("" ::: "memory");
;         } else {
;             asm volatile("buffer_inv sc1" ::: "memory");
;             XB_SPIN(xb_ld(&bar[XB_XGEN(b.x)]) == gen, bar);
;             asm volatile("" ::: "memory");
;             asm volatile("s_waitcnt vmcnt(0)" ::: "memory");
;         }
.LBB0_33:
	s_or_b64 exec, exec, s[10:11]
	v_cvt_f32_u32_e32 v5, v3
	s_waitcnt vmcnt(0)
	v_readfirstlane_b32 s0, v4
	v_sub_u32_e32 v4, 0, v3
	v_rcp_iflag_f32_e32 v5, v5
	v_add_u32_e32 v6, s0, v2
	v_mul_f32_e32 v5, 0x4f7ffffe, v5
	v_cvt_u32_f32_e32 v5, v5
	v_mul_lo_u32 v2, v4, v5
	v_mul_hi_u32 v2, v5, v2
	v_add_u32_e32 v2, v5, v2
	v_mul_hi_u32 v2, v6, v2
	v_mul_lo_u32 v4, v2, v3
	v_sub_u32_e32 v4, v6, v4
	v_add_u32_e32 v5, 1, v2
	v_cmp_ge_u32_e32 vcc, v4, v3
	s_nop 1
	v_cndmask_b32_e32 v2, v2, v5, vcc
	v_sub_u32_e32 v5, v4, v3
	v_cndmask_b32_e32 v4, v4, v5, vcc
	v_add_u32_e32 v5, 1, v2
	v_cmp_ge_u32_e32 vcc, v4, v3
	v_add_u32_e32 v4, 1, v6
	s_nop 0
	v_cndmask_b32_e32 v2, v2, v5, vcc
	v_mul_lo_u32 v5, v3, v2
	v_readfirstlane_b32 s98, v2
	v_add_u32_e32 v3, v5, v3
	v_cmp_ne_u32_e32 vcc, v4, v3
	s_and_saveexec_b64 s[0:1], vcc
	s_xor_b64 s[0:1], exec, s[0:1]
	s_cbranch_execz .LBB0_47
	buffer_inv sc1
	v_lshl_add_u32 v2, v2, 1, 1
	s_waitcnt lgkmcnt(0)
	v_mov_b32_e32 v1, 0x2000
	global_load_dword v1, v1, s[4:5] offset:1024 sc1
	s_add_u32 s14, s4, 0x2400
	s_addc_u32 s15, s5, 0
	s_waitcnt vmcnt(0)
	v_cmp_lt_u32_e32 vcc, v1, v2
	s_and_saveexec_b64 s[10:11], vcc
	s_cbranch_execz .LBB0_46
	s_add_u32 s12, s82, 0x4200
	s_addc_u32 s13, s83, 0
	s_mov_b32 s3, 1
	s_mov_b64 s[16:17], 0
	v_mov_b32_e32 v1, 0
	s_branch .LBB0_37

; __device__ __forceinline__ unsigned xb_ld(unsigned* p)              { return __hip_atomic_load(p, __ATOMIC_RELAXED, __HIP_MEMORY_SCOPE_AGENT); }
; #define XB_SPIN(cond, bar) do { unsigned _sp = 0; while (cond) { __builtin_amdgcn_s_sleep(1); \
;     if ((++_sp & 255u) == 0u) { if (xb_ld(&(bar)[XB_TMO])) break; if (_sp > XB_SPIN_CAP) { atomicAdd(&(bar)[XB_TMO], 1u); break; } } } } while (0)
; __device__ __forceinline__ void xcd_barrier(const XcdBarrier& b) {
;     ...
;             XB_SPIN(xb_ld(&bar[XB_XGEN(b.x)]) == gen, bar);
.LBB0_39:
	global_load_dword v3, v1, s[14:15] sc1
	s_add_i32 s3, s3, 1
	s_mov_b64 s[22:23], -1
	s_waitcnt vmcnt(0)
	v_cmp_ge_u32_e32 vcc, v3, v2
	s_orn2_b64 s[20:21], vcc, exec
	s_branch .LBB0_36

; __device__ __forceinline__ unsigned xb_ld(unsigned* p)              { return __hip_atomic_load(p, __ATOMIC_RELAXED, __HIP_MEMORY_SCOPE_AGENT); }
; __device__ __forceinline__ unsigned xb_add(unsigned* p, unsigned v) { return __hip_atomic_fetch_add(p, v, __ATOMIC_RELAXED, __HIP_MEMORY_SCOPE_AGENT); }
; #define XB_SPIN(cond, bar) do { unsigned _sp = 0; while (cond) { __builtin_amdgcn_s_sleep(1); \
;     if ((++_sp & 255u) == 0u) { if (xb_ld(&(bar)[XB_TMO])) break; if (_sp > XB_SPIN_CAP) { atomicAdd(&(bar)[XB_TMO], 1u); break; } } } } while (0)
; __device__ __forceinline__ void xcd_barrier(const XcdBarrier& b) {
;     ...
;             asm volatile("buffer_inv sc1" ::: "memory");
;             __builtin_amdgcn_fence(__ATOMIC_RELEASE, "agent");
;             asm volatile("s_waitcnt vmcnt(0)" ::: "memory");
;             const unsigned og = xb_add(&bar[XB_TOP], 1u);
;             const unsigned tg = og / nx;
;             if (og + 1u == (tg + 1u) * nx) xb_add(&bar[XB_TOPGEN], 1u);
;             else XB_SPIN(xb_ld(&bar[XB_TOPGEN]) == tg, bar);
;             asm volatile("" ::: "memory");
;             xb_add(&bar[XB_XGEN(b.x)], 1u);
;             asm volatile("" ::: "memory");
.LBB0_50:
	s_or_b64 exec, exec, s[10:11]
	v_cvt_f32_u32_e32 v4, v1
	s_waitcnt vmcnt(0)
	v_readfirstlane_b32 s0, v3
	s_add_u32 s10, s82, 0x7500
	s_addc_u32 s11, s83, 0
	v_rcp_iflag_f32_e32 v4, v4
	v_add_u32_e32 v2, s0, v2
	v_add_u32_e32 v5, 1, v2
	s_mov_b64 s[12:13], -1
	v_mul_f32_e32 v3, 0x4f7ffffe, v4
	v_cvt_u32_f32_e32 v3, v3
	v_sub_u32_e32 v4, 0, v1
	v_mul_lo_u32 v4, v4, v3
	v_mul_hi_u32 v4, v3, v4
	v_add_u32_e32 v3, v3, v4
	v_mul_hi_u32 v3, v2, v3
	v_mul_lo_u32 v4, v3, v1
	v_sub_u32_e32 v2, v2, v4
	v_add_u32_e32 v6, 1, v3
	v_cmp_ge_u32_e32 vcc, v2, v1
	v_sub_u32_e32 v4, v2, v1
	s_nop 0
	v_cndmask_b32_e32 v3, v3, v6, vcc
	v_cndmask_b32_e32 v2, v2, v4, vcc
	v_add_u32_e32 v4, 1, v3
	v_cmp_ge_u32_e32 vcc, v2, v1
	s_nop 1
	v_cndmask_b32_e32 v4, v3, v4, vcc
	v_mul_lo_u32 v2, v1, v4
	v_add_u32_e32 v1, v2, v1
	v_cmp_ne_u32_e32 vcc, v5, v1
	v_mov_b64_e32 v[2:3], s[10:11]
	s_and_saveexec_b64 s[0:1], vcc
	s_cbranch_execz .LBB0_62
	s_add_u32 s10, s4, 0x2400
	s_addc_u32 s11, s5, 0
	v_mov_b32_e32 v4, s98
	v_lshl_add_u32 v4, v4, 1, 1
	v_mov_b32_e32 v1, 0
	global_load_dword v2, v1, s[10:11] sc1
	s_mov_b64 s[16:17], 0
	s_waitcnt vmcnt(0)
	v_cmp_lt_u32_e32 vcc, v2, v4
	s_and_saveexec_b64 s[14:15], vcc
	s_cbranch_execz .LBB0_61
	s_add_u32 s12, s82, 0x4200
	s_addc_u32 s13, s83, 0
	s_mov_b32 s3, 1
	s_branch .LBB0_54

; __device__ __forceinline__ unsigned xb_ld(unsigned* p)              { return __hip_atomic_load(p, __ATOMIC_RELAXED, __HIP_MEMORY_SCOPE_AGENT); }
; #define XB_SPIN(cond, bar) do { unsigned _sp = 0; while (cond) { __builtin_amdgcn_s_sleep(1); \
;     if ((++_sp & 255u) == 0u) { if (xb_ld(&(bar)[XB_TMO])) break; if (_sp > XB_SPIN_CAP) { atomicAdd(&(bar)[XB_TMO], 1u); break; } } } } while (0)
; __device__ __forceinline__ void xcd_barrier(const XcdBarrier& b) {
;     ...
;             else XB_SPIN(xb_ld(&bar[XB_TOPGEN]) == tg, bar);
.LBB0_56:
	global_load_dword v2, v1, s[10:11] sc1
	s_add_i32 s3, s3, 1
	s_mov_b64 s[20:21], -1
	s_waitcnt vmcnt(0)
	v_cmp_ge_u32_e32 vcc, v2, v4
	s_orn2_b64 s[24:25], vcc, exec
	s_branch .LBB0_53

; __device__ __forceinline__ unsigned xb_ld(unsigned* p)              { return __hip_atomic_load(p, __ATOMIC_RELAXED, __HIP_MEMORY_SCOPE_AGENT); }
; __device__ __forceinline__ unsigned xb_add(unsigned* p, unsigned v) { return __hip_atomic_fetch_add(p, v, __ATOMIC_RELAXED, __HIP_MEMORY_SCOPE_AGENT); }
; #define XB_SPIN(cond, bar) do { unsigned _sp = 0; while (cond) { __builtin_amdgcn_s_sleep(1); \
;     if ((++_sp & 255u) == 0u) { if (xb_ld(&(bar)[XB_TMO])) break; if (_sp > XB_SPIN_CAP) { atomicAdd(&(bar)[XB_TMO], 1u); break; } } } } while (0)
; __device__ __forceinline__ void xcd_barrier(const XcdBarrier& b) {
;     ...
;             const unsigned og = xb_add(&bar[XB_TOP], 1u);
;             const unsigned tg = og / nx;
;             if (og + 1u == (tg + 1u) * nx) xb_add(&bar[XB_TOPGEN], 1u);
;             else XB_SPIN(xb_ld(&bar[XB_TOPGEN]) == tg, bar);
;             asm volatile("" ::: "memory");
;             xb_add(&bar[XB_XGEN(b.x)], 1u);
.LBB0_62:
	s_or_b64 exec, exec, s[0:1]
	s_and_saveexec_b64 s[0:1], s[12:13]
	s_cbranch_execz .LBB0_64
	v_mov_b32_e32 v1, 1
	global_atomic_add v[2:3], v1, off
	v_mov_b32_e32 v4, 0x6400
	global_atomic_add v4, v1, s[82:83]
	global_atomic_add v4, v1, s[82:83] offset:256
	global_atomic_add v4, v1, s[82:83] offset:512
	global_atomic_add v4, v1, s[82:83] offset:768
	global_atomic_add v4, v1, s[82:83] offset:1024
	global_atomic_add v4, v1, s[82:83] offset:1280
	global_atomic_add v4, v1, s[82:83] offset:1536
	global_atomic_add v4, v1, s[82:83] offset:1792
	global_atomic_add v4, v1, s[82:83] offset:2048
	global_atomic_add v4, v1, s[82:83] offset:2304
	global_atomic_add v4, v1, s[82:83] offset:2560
	global_atomic_add v4, v1, s[82:83] offset:2816
	global_atomic_add v4, v1, s[82:83] offset:3072
	global_atomic_add v4, v1, s[82:83] offset:3328
	global_atomic_add v4, v1, s[82:83] offset:3584
	global_atomic_add v4, v1, s[82:83] offset:3840

; __device__ __forceinline__ unsigned xb_ld(unsigned* p)              { return __hip_atomic_load(p, __ATOMIC_RELAXED, __HIP_MEMORY_SCOPE_AGENT); }
; __device__ __forceinline__ unsigned xb_add(unsigned* p, unsigned v) { return __hip_atomic_fetch_add(p, v, __ATOMIC_RELAXED, __HIP_MEMORY_SCOPE_AGENT); }
; #define XB_SPIN(cond, bar) do { unsigned _sp = 0; while (cond) { __builtin_amdgcn_s_sleep(1); \
;     if ((++_sp & 255u) == 0u) { if (xb_ld(&(bar)[XB_TMO])) break; if (_sp > XB_SPIN_CAP) { atomicAdd(&(bar)[XB_TMO], 1u); break; } } } } while (0)
; __device__ __forceinline__ void xcd_barrier(const XcdBarrier& b) {
;     ...
;         const unsigned old = xb_add(&bar[XB_XSUB(b.x)], 1u);
;         const unsigned gen = old / nloc;
;         if (old + 1u == (gen + 1u) * nloc) {
;             asm volatile("buffer_inv sc1" ::: "memory");
;             __builtin_amdgcn_fence(__ATOMIC_RELEASE, "agent");
;             asm volatile("s_waitcnt vmcnt(0)" ::: "memory");
;             const unsigned og = xb_add(&bar[XB_TOP], 1u);
;             const unsigned tg = og / nx;
;             if (og + 1u == (tg + 1u) * nx) xb_add(&bar[XB_TOPGEN], 1u);
;             else XB_SPIN(xb_ld(&bar[XB_TOPGEN]) == tg, bar);
;             asm volatile("" ::: "memory");
;             xb_add(&bar[XB_XGEN(b.x)], 1u);
;             asm volatile("" ::: "memory");
;         } else {
;             asm volatile("buffer_inv sc1" ::: "memory");
;             XB_SPIN(xb_ld(&bar[XB_XGEN(b.x)]) == gen, bar);
;             asm volatile("" ::: "memory");
;             asm volatile("s_waitcnt vmcnt(0)" ::: "memory");
;         }
.LBB0_103:
	s_or_b64 exec, exec, s[10:11]
	v_cvt_f32_u32_e32 v5, v3
	s_waitcnt vmcnt(0)
	v_readfirstlane_b32 s3, v4
	v_sub_u32_e32 v4, 0, v3
	v_rcp_iflag_f32_e32 v5, v5
	v_add_u32_e32 v6, s3, v2
	v_mul_f32_e32 v5, 0x4f7ffffe, v5
	v_cvt_u32_f32_e32 v5, v5
	v_mul_lo_u32 v2, v4, v5
	v_mul_hi_u32 v2, v5, v2
	v_add_u32_e32 v2, v5, v2
	v_mul_hi_u32 v2, v6, v2
	v_mul_lo_u32 v4, v2, v3
	v_sub_u32_e32 v4, v6, v4
	v_add_u32_e32 v5, 1, v2
	v_cmp_ge_u32_e32 vcc, v4, v3
	s_nop 1
	v_cndmask_b32_e32 v2, v2, v5, vcc
	v_sub_u32_e32 v5, v4, v3
	v_cndmask_b32_e32 v4, v4, v5, vcc
	v_add_u32_e32 v5, 1, v2
	v_cmp_ge_u32_e32 vcc, v4, v3
	v_add_u32_e32 v4, 1, v6
	s_nop 0
	v_cndmask_b32_e32 v2, v2, v5, vcc
	v_mul_lo_u32 v5, v3, v2
	v_readfirstlane_b32 s98, v2
	v_add_u32_e32 v3, v5, v3
	v_cmp_ne_u32_e32 vcc, v4, v3
	s_and_saveexec_b64 s[8:9], vcc
	s_xor_b64 s[8:9], exec, s[8:9]
	s_cbranch_execz .LBB0_117
	buffer_inv sc1
	v_lshl_add_u32 v2, v2, 1, 1
	s_waitcnt lgkmcnt(0)
	v_mov_b32_e32 v1, 0x2000
	global_load_dword v1, v1, s[4:5] offset:1024 sc1
	s_add_u32 s14, s4, 0x2400
	s_addc_u32 s15, s5, 0
	s_waitcnt vmcnt(0)
	v_cmp_lt_u32_e32 vcc, v1, v2
	s_and_saveexec_b64 s[10:11], vcc
	s_cbranch_execz .LBB0_116
	s_add_u32 s12, s82, 0x4200
	s_addc_u32 s13, s83, 0
	s_mov_b32 s3, 1
	s_mov_b64 s[16:17], 0
	v_mov_b32_e32 v1, 0
	s_branch .LBB0_107

; __device__ __forceinline__ unsigned xb_ld(unsigned* p)              { return __hip_atomic_load(p, __ATOMIC_RELAXED, __HIP_MEMORY_SCOPE_AGENT); }
; __device__ __forceinline__ unsigned xb_add(unsigned* p, unsigned v) { return __hip_atomic_fetch_add(p, v, __ATOMIC_RELAXED, __HIP_MEMORY_SCOPE_AGENT); }
; #define XB_SPIN(cond, bar) do { unsigned _sp = 0; while (cond) { __builtin_amdgcn_s_sleep(1); \
;     if ((++_sp & 255u) == 0u) { if (xb_ld(&(bar)[XB_TMO])) break; if (_sp > XB_SPIN_CAP) { atomicAdd(&(bar)[XB_TMO], 1u); break; } } } } while (0)
; __device__ __forceinline__ void xcd_barrier(const XcdBarrier& b) {
;     ...
;             asm volatile("buffer_inv sc1" ::: "memory");
;             __builtin_amdgcn_fence(__ATOMIC_RELEASE, "agent");
;             asm volatile("s_waitcnt vmcnt(0)" ::: "memory");
;             const unsigned og = xb_add(&bar[XB_TOP], 1u);
;             const unsigned tg = og / nx;
;             if (og + 1u == (tg + 1u) * nx) xb_add(&bar[XB_TOPGEN], 1u);
;             else XB_SPIN(xb_ld(&bar[XB_TOPGEN]) == tg, bar);
;             asm volatile("" ::: "memory");
;             xb_add(&bar[XB_XGEN(b.x)], 1u);
;             asm volatile("" ::: "memory");
.LBB0_120:
	s_or_b64 exec, exec, s[10:11]
	v_cvt_f32_u32_e32 v4, v1
	s_waitcnt vmcnt(0)
	v_readfirstlane_b32 s3, v3
	s_add_u32 s10, s82, 0x7500
	s_addc_u32 s11, s83, 0
	v_rcp_iflag_f32_e32 v4, v4
	v_add_u32_e32 v2, s3, v2
	v_add_u32_e32 v5, 1, v2
	s_mov_b64 s[12:13], -1
	v_mul_f32_e32 v3, 0x4f7ffffe, v4
	v_cvt_u32_f32_e32 v3, v3
	v_sub_u32_e32 v4, 0, v1
	v_mul_lo_u32 v4, v4, v3
	v_mul_hi_u32 v4, v3, v4
	v_add_u32_e32 v3, v3, v4
	v_mul_hi_u32 v3, v2, v3
	v_mul_lo_u32 v4, v3, v1
	v_sub_u32_e32 v2, v2, v4
	v_add_u32_e32 v6, 1, v3
	v_cmp_ge_u32_e32 vcc, v2, v1
	v_sub_u32_e32 v4, v2, v1
	s_nop 0
	v_cndmask_b32_e32 v3, v3, v6, vcc
	v_cndmask_b32_e32 v2, v2, v4, vcc
	v_add_u32_e32 v4, 1, v3
	v_cmp_ge_u32_e32 vcc, v2, v1
	s_nop 1
	v_cndmask_b32_e32 v4, v3, v4, vcc
	v_mul_lo_u32 v2, v1, v4
	v_add_u32_e32 v1, v2, v1
	v_cmp_ne_u32_e32 vcc, v5, v1
	v_mov_b64_e32 v[2:3], s[10:11]
	s_and_saveexec_b64 s[8:9], vcc
	s_cbranch_execz .LBB0_132
	s_add_u32 s10, s4, 0x2400
	s_addc_u32 s11, s5, 0
	v_mov_b32_e32 v4, s98
	v_lshl_add_u32 v4, v4, 1, 1
	v_mov_b32_e32 v1, 0
	global_load_dword v2, v1, s[10:11] sc1
	s_mov_b64 s[16:17], 0
	s_waitcnt vmcnt(0)
	v_cmp_lt_u32_e32 vcc, v2, v4
	s_and_saveexec_b64 s[14:15], vcc
	s_cbranch_execz .LBB0_131
	s_add_u32 s12, s82, 0x4200
	s_addc_u32 s13, s83, 0
	s_mov_b32 s3, 1
	s_branch .LBB0_124

; __device__ __forceinline__ unsigned xb_ld(unsigned* p)              { return __hip_atomic_load(p, __ATOMIC_RELAXED, __HIP_MEMORY_SCOPE_AGENT); }
; __device__ __forceinline__ unsigned xb_add(unsigned* p, unsigned v) { return __hip_atomic_fetch_add(p, v, __ATOMIC_RELAXED, __HIP_MEMORY_SCOPE_AGENT); }
; #define XB_SPIN(cond, bar) do { unsigned _sp = 0; while (cond) { __builtin_amdgcn_s_sleep(1); \
;     if ((++_sp & 255u) == 0u) { if (xb_ld(&(bar)[XB_TMO])) break; if (_sp > XB_SPIN_CAP) { atomicAdd(&(bar)[XB_TMO], 1u); break; } } } } while (0)
; __device__ __forceinline__ void xcd_barrier(const XcdBarrier& b) {
;     ...
;             const unsigned og = xb_add(&bar[XB_TOP], 1u);
;             const unsigned tg = og / nx;
;             if (og + 1u == (tg + 1u) * nx) xb_add(&bar[XB_TOPGEN], 1u);
;             else XB_SPIN(xb_ld(&bar[XB_TOPGEN]) == tg, bar);
;             asm volatile("" ::: "memory");
;             xb_add(&bar[XB_XGEN(b.x)], 1u);
.LBB0_132:
	s_or_b64 exec, exec, s[8:9]
	s_and_saveexec_b64 s[8:9], s[12:13]
	s_cbranch_execz .LBB0_134
	v_mov_b32_e32 v1, 1
	global_atomic_add v[2:3], v1, off
	v_mov_b32_e32 v4, 0x6400
	global_atomic_add v4, v1, s[82:83]
	global_atomic_add v4, v1, s[82:83] offset:256
	global_atomic_add v4, v1, s[82:83] offset:512
	global_atomic_add v4, v1, s[82:83] offset:768
	global_atomic_add v4, v1, s[82:83] offset:1024
	global_atomic_add v4, v1, s[82:83] offset:1280
	global_atomic_add v4, v1, s[82:83] offset:1536
	global_atomic_add v4, v1, s[82:83] offset:1792
	global_atomic_add v4, v1, s[82:83] offset:2048
	global_atomic_add v4, v1, s[82:83] offset:2304
	global_atomic_add v4, v1, s[82:83] offset:2560
	global_atomic_add v4, v1, s[82:83] offset:2816
	global_atomic_add v4, v1, s[82:83] offset:3072
	global_atomic_add v4, v1, s[82:83] offset:3328
	global_atomic_add v4, v1, s[82:83] offset:3584
	global_atomic_add v4, v1, s[82:83] offset:3840

; __device__ __forceinline__ unsigned xb_ld(unsigned* p)              { return __hip_atomic_load(p, __ATOMIC_RELAXED, __HIP_MEMORY_SCOPE_AGENT); }
; __device__ __forceinline__ unsigned xb_add(unsigned* p, unsigned v) { return __hip_atomic_fetch_add(p, v, __ATOMIC_RELAXED, __HIP_MEMORY_SCOPE_AGENT); }
; #define XB_SPIN(cond, bar) do { unsigned _sp = 0; while (cond) { __builtin_amdgcn_s_sleep(1); \
;     if ((++_sp & 255u) == 0u) { if (xb_ld(&(bar)[XB_TMO])) break; if (_sp > XB_SPIN_CAP) { atomicAdd(&(bar)[XB_TMO], 1u); break; } } } } while (0)
; __device__ __forceinline__ void xcd_barrier(const XcdBarrier& b) {
;     ...
;         const unsigned old = xb_add(&bar[XB_XSUB(b.x)], 1u);
;         const unsigned gen = old / nloc;
;         if (old + 1u == (gen + 1u) * nloc) {
;             asm volatile("buffer_inv sc1" ::: "memory");
;             __builtin_amdgcn_fence(__ATOMIC_RELEASE, "agent");
;             asm volatile("s_waitcnt vmcnt(0)" ::: "memory");
;             const unsigned og = xb_add(&bar[XB_TOP], 1u);
;             const unsigned tg = og / nx;
;             if (og + 1u == (tg + 1u) * nx) xb_add(&bar[XB_TOPGEN], 1u);
;             else XB_SPIN(xb_ld(&bar[XB_TOPGEN]) == tg, bar);
;             asm volatile("" ::: "memory");
;             xb_add(&bar[XB_XGEN(b.x)], 1u);
;             asm volatile("" ::: "memory");
;         } else {
;             asm volatile("buffer_inv sc1" ::: "memory");
;             XB_SPIN(xb_ld(&bar[XB_XGEN(b.x)]) == gen, bar);
;             asm volatile("" ::: "memory");
;             asm volatile("s_waitcnt vmcnt(0)" ::: "memory");
;         }
.LBB0_183:
	s_or_b64 exec, exec, s[10:11]
	v_cvt_f32_u32_e32 v5, v3
	s_waitcnt vmcnt(0)
	v_readfirstlane_b32 s8, v4
	v_sub_u32_e32 v4, 0, v3
	v_rcp_iflag_f32_e32 v5, v5
	v_add_u32_e32 v6, s8, v2
	v_mul_f32_e32 v5, 0x4f7ffffe, v5
	v_cvt_u32_f32_e32 v5, v5
	v_mul_lo_u32 v2, v4, v5
	v_mul_hi_u32 v2, v5, v2
	v_add_u32_e32 v2, v5, v2
	v_mul_hi_u32 v2, v6, v2
	v_mul_lo_u32 v4, v2, v3
	v_sub_u32_e32 v4, v6, v4
	v_add_u32_e32 v5, 1, v2
	v_cmp_ge_u32_e32 vcc, v4, v3
	s_nop 1
	v_cndmask_b32_e32 v2, v2, v5, vcc
	v_sub_u32_e32 v5, v4, v3
	v_cndmask_b32_e32 v4, v4, v5, vcc
	v_add_u32_e32 v5, 1, v2
	v_cmp_ge_u32_e32 vcc, v4, v3
	v_add_u32_e32 v4, 1, v6
	s_nop 0
	v_cndmask_b32_e32 v2, v2, v5, vcc
	v_mul_lo_u32 v5, v3, v2
	v_readfirstlane_b32 s98, v2
	v_add_u32_e32 v3, v5, v3
	v_cmp_ne_u32_e32 vcc, v4, v3
	s_and_saveexec_b64 s[8:9], vcc
	s_xor_b64 s[8:9], exec, s[8:9]
	s_cbranch_execz .LBB0_197
	buffer_inv sc1
	v_lshl_add_u32 v2, v2, 1, 1
	s_waitcnt lgkmcnt(0)
	v_mov_b32_e32 v1, 0x2000
	global_load_dword v1, v1, s[4:5] offset:1024 sc1
	s_add_u32 s16, s4, 0x2400
	s_addc_u32 s17, s5, 0
	s_waitcnt vmcnt(0)
	v_cmp_lt_u32_e32 vcc, v1, v2
	s_and_saveexec_b64 s[10:11], vcc
	s_cbranch_execz .LBB0_196
	s_add_u32 s14, s82, 0x4200
	s_addc_u32 s15, s83, 0
	s_mov_b32 s28, 1
	s_mov_b64 s[18:19], 0
	v_mov_b32_e32 v1, 0
	s_branch .LBB0_187

; __device__ __forceinline__ unsigned xb_ld(unsigned* p)              { return __hip_atomic_load(p, __ATOMIC_RELAXED, __HIP_MEMORY_SCOPE_AGENT); }
; #define XB_SPIN(cond, bar) do { unsigned _sp = 0; while (cond) { __builtin_amdgcn_s_sleep(1); \
;     if ((++_sp & 255u) == 0u) { if (xb_ld(&(bar)[XB_TMO])) break; if (_sp > XB_SPIN_CAP) { atomicAdd(&(bar)[XB_TMO], 1u); break; } } } } while (0)
; __device__ __forceinline__ void xcd_barrier(const XcdBarrier& b) {
;     ...
;             XB_SPIN(xb_ld(&bar[XB_XGEN(b.x)]) == gen, bar);
.LBB0_189:
	global_load_dword v3, v1, s[16:17] sc1
	s_add_i32 s28, s28, 1
	s_mov_b64 s[24:25], -1
	s_waitcnt vmcnt(0)
	v_cmp_ge_u32_e32 vcc, v3, v2
	s_orn2_b64 s[22:23], vcc, exec
	s_branch .LBB0_186

; __device__ __forceinline__ unsigned xb_ld(unsigned* p)              { return __hip_atomic_load(p, __ATOMIC_RELAXED, __HIP_MEMORY_SCOPE_AGENT); }
; __device__ __forceinline__ unsigned xb_add(unsigned* p, unsigned v) { return __hip_atomic_fetch_add(p, v, __ATOMIC_RELAXED, __HIP_MEMORY_SCOPE_AGENT); }
; #define XB_SPIN(cond, bar) do { unsigned _sp = 0; while (cond) { __builtin_amdgcn_s_sleep(1); \
;     if ((++_sp & 255u) == 0u) { if (xb_ld(&(bar)[XB_TMO])) break; if (_sp > XB_SPIN_CAP) { atomicAdd(&(bar)[XB_TMO], 1u); break; } } } } while (0)
; __device__ __forceinline__ void xcd_barrier(const XcdBarrier& b) {
;     ...
;             asm volatile("buffer_inv sc1" ::: "memory");
;             __builtin_amdgcn_fence(__ATOMIC_RELEASE, "agent");
;             asm volatile("s_waitcnt vmcnt(0)" ::: "memory");
;             const unsigned og = xb_add(&bar[XB_TOP], 1u);
;             const unsigned tg = og / nx;
;             if (og + 1u == (tg + 1u) * nx) xb_add(&bar[XB_TOPGEN], 1u);
;             else XB_SPIN(xb_ld(&bar[XB_TOPGEN]) == tg, bar);
;             asm volatile("" ::: "memory");
;             xb_add(&bar[XB_XGEN(b.x)], 1u);
;             asm volatile("" ::: "memory");
.LBB0_200:
	s_or_b64 exec, exec, s[10:11]
	v_cvt_f32_u32_e32 v4, v1
	s_waitcnt vmcnt(0)
	v_readfirstlane_b32 s8, v3
	s_add_u32 s10, s82, 0x7500
	s_addc_u32 s11, s83, 0
	v_rcp_iflag_f32_e32 v4, v4
	v_add_u32_e32 v2, s8, v2
	v_add_u32_e32 v5, 1, v2
	s_mov_b64 s[14:15], -1
	v_mul_f32_e32 v3, 0x4f7ffffe, v4
	v_cvt_u32_f32_e32 v3, v3
	v_sub_u32_e32 v4, 0, v1
	v_mul_lo_u32 v4, v4, v3
	v_mul_hi_u32 v4, v3, v4
	v_add_u32_e32 v3, v3, v4
	v_mul_hi_u32 v3, v2, v3
	v_mul_lo_u32 v4, v3, v1
	v_sub_u32_e32 v2, v2, v4
	v_add_u32_e32 v6, 1, v3
	v_cmp_ge_u32_e32 vcc, v2, v1
	v_sub_u32_e32 v4, v2, v1
	s_nop 0
	v_cndmask_b32_e32 v3, v3, v6, vcc
	v_cndmask_b32_e32 v2, v2, v4, vcc
	v_add_u32_e32 v4, 1, v3
	v_cmp_ge_u32_e32 vcc, v2, v1
	s_nop 1
	v_cndmask_b32_e32 v4, v3, v4, vcc
	v_mul_lo_u32 v2, v1, v4
	v_add_u32_e32 v1, v2, v1
	v_cmp_ne_u32_e32 vcc, v5, v1
	v_mov_b64_e32 v[2:3], s[10:11]
	s_and_saveexec_b64 s[8:9], vcc
	s_cbranch_execz .LBB0_212
	s_add_u32 s10, s4, 0x2400
	s_addc_u32 s11, s5, 0
	v_mov_b32_e32 v4, s98
	v_lshl_add_u32 v4, v4, 1, 1
	v_mov_b32_e32 v1, 0
	global_load_dword v2, v1, s[10:11] sc1
	s_mov_b64 s[18:19], 0
	s_waitcnt vmcnt(0)
	v_cmp_lt_u32_e32 vcc, v2, v4
	s_and_saveexec_b64 s[16:17], vcc
	s_cbranch_execz .LBB0_211
	s_add_u32 s14, s82, 0x4200
	s_addc_u32 s15, s83, 0
	s_mov_b32 s28, 1
	s_branch .LBB0_204

; __device__ __forceinline__ unsigned xb_ld(unsigned* p)              { return __hip_atomic_load(p, __ATOMIC_RELAXED, __HIP_MEMORY_SCOPE_AGENT); }
; #define XB_SPIN(cond, bar) do { unsigned _sp = 0; while (cond) { __builtin_amdgcn_s_sleep(1); \
;     if ((++_sp & 255u) == 0u) { if (xb_ld(&(bar)[XB_TMO])) break; if (_sp > XB_SPIN_CAP) { atomicAdd(&(bar)[XB_TMO], 1u); break; } } } } while (0)
; __device__ __forceinline__ void xcd_barrier(const XcdBarrier& b) {
;     ...
;             else XB_SPIN(xb_ld(&bar[XB_TOPGEN]) == tg, bar);
.LBB0_206:
	global_load_dword v2, v1, s[10:11] sc1
	s_add_i32 s28, s28, 1
	s_mov_b64 s[22:23], -1
	s_waitcnt vmcnt(0)
	v_cmp_ge_u32_e32 vcc, v2, v4
	s_orn2_b64 s[26:27], vcc, exec
	s_branch .LBB0_203

; __device__ __forceinline__ unsigned xb_ld(unsigned* p)              { return __hip_atomic_load(p, __ATOMIC_RELAXED, __HIP_MEMORY_SCOPE_AGENT); }
; __device__ __forceinline__ unsigned xb_add(unsigned* p, unsigned v) { return __hip_atomic_fetch_add(p, v, __ATOMIC_RELAXED, __HIP_MEMORY_SCOPE_AGENT); }
; #define XB_SPIN(cond, bar) do { unsigned _sp = 0; while (cond) { __builtin_amdgcn_s_sleep(1); \
;     if ((++_sp & 255u) == 0u) { if (xb_ld(&(bar)[XB_TMO])) break; if (_sp > XB_SPIN_CAP) { atomicAdd(&(bar)[XB_TMO], 1u); break; } } } } while (0)
; __device__ __forceinline__ void xcd_barrier(const XcdBarrier& b) {
;     ...
;             const unsigned og = xb_add(&bar[XB_TOP], 1u);
;             const unsigned tg = og / nx;
;             if (og + 1u == (tg + 1u) * nx) xb_add(&bar[XB_TOPGEN], 1u);
;             else XB_SPIN(xb_ld(&bar[XB_TOPGEN]) == tg, bar);
;             asm volatile("" ::: "memory");
;             xb_add(&bar[XB_XGEN(b.x)], 1u);
.LBB0_212:
	s_or_b64 exec, exec, s[8:9]
	s_and_saveexec_b64 s[8:9], s[14:15]
	s_cbranch_execz .LBB0_214
	v_mov_b32_e32 v1, 1
	global_atomic_add v[2:3], v1, off
	v_mov_b32_e32 v4, 0x6400
	global_atomic_add v4, v1, s[82:83]
	global_atomic_add v4, v1, s[82:83] offset:256
	global_atomic_add v4, v1, s[82:83] offset:512
	global_atomic_add v4, v1, s[82:83] offset:768
	global_atomic_add v4, v1, s[82:83] offset:1024
	global_atomic_add v4, v1, s[82:83] offset:1280
	global_atomic_add v4, v1, s[82:83] offset:1536
	global_atomic_add v4, v1, s[82:83] offset:1792
	global_atomic_add v4, v1, s[82:83] offset:2048
	global_atomic_add v4, v1, s[82:83] offset:2304
	global_atomic_add v4, v1, s[82:83] offset:2560
	global_atomic_add v4, v1, s[82:83] offset:2816
	global_atomic_add v4, v1, s[82:83] offset:3072
	global_atomic_add v4, v1, s[82:83] offset:3328
	global_atomic_add v4, v1, s[82:83] offset:3584
	global_atomic_add v4, v1, s[82:83] offset:3840

; __device__ __forceinline__ unsigned xb_ld(unsigned* p)              { return __hip_atomic_load(p, __ATOMIC_RELAXED, __HIP_MEMORY_SCOPE_AGENT); }
; __device__ __forceinline__ unsigned xb_add(unsigned* p, unsigned v) { return __hip_atomic_fetch_add(p, v, __ATOMIC_RELAXED, __HIP_MEMORY_SCOPE_AGENT); }
; #define XB_SPIN(cond, bar) do { unsigned _sp = 0; while (cond) { __builtin_amdgcn_s_sleep(1); \
;     if ((++_sp & 255u) == 0u) { if (xb_ld(&(bar)[XB_TMO])) break; if (_sp > XB_SPIN_CAP) { atomicAdd(&(bar)[XB_TMO], 1u); break; } } } } while (0)
; __device__ __forceinline__ void xcd_barrier(const XcdBarrier& b) {
;     ...
;         const unsigned old = xb_add(&bar[XB_XSUB(b.x)], 1u);
;         const unsigned gen = old / nloc;
;         if (old + 1u == (gen + 1u) * nloc) {
;             asm volatile("buffer_inv sc1" ::: "memory");
;             __builtin_amdgcn_fence(__ATOMIC_RELEASE, "agent");
;             asm volatile("s_waitcnt vmcnt(0)" ::: "memory");
;             const unsigned og = xb_add(&bar[XB_TOP], 1u);
;             const unsigned tg = og / nx;
;             if (og + 1u == (tg + 1u) * nx) xb_add(&bar[XB_TOPGEN], 1u);
;             else XB_SPIN(xb_ld(&bar[XB_TOPGEN]) == tg, bar);
;             asm volatile("" ::: "memory");
;             xb_add(&bar[XB_XGEN(b.x)], 1u);
;             asm volatile("" ::: "memory");
;         } else {
;             asm volatile("buffer_inv sc1" ::: "memory");
;             XB_SPIN(xb_ld(&bar[XB_XGEN(b.x)]) == gen, bar);
;             asm volatile("" ::: "memory");
;             asm volatile("s_waitcnt vmcnt(0)" ::: "memory");
;         }
.LBB0_626:
	s_or_b64 exec, exec, s[10:11]
	v_cvt_f32_u32_e32 v5, v3
	s_waitcnt vmcnt(0)
	v_readfirstlane_b32 s8, v4
	v_sub_u32_e32 v4, 0, v3
	v_rcp_iflag_f32_e32 v5, v5
	v_add_u32_e32 v6, s8, v2
	v_mul_f32_e32 v5, 0x4f7ffffe, v5
	v_cvt_u32_f32_e32 v5, v5
	v_mul_lo_u32 v2, v4, v5
	v_mul_hi_u32 v2, v5, v2
	v_add_u32_e32 v2, v5, v2
	v_mul_hi_u32 v2, v6, v2
	v_mul_lo_u32 v4, v2, v3
	v_sub_u32_e32 v4, v6, v4
	v_add_u32_e32 v5, 1, v2
	v_cmp_ge_u32_e32 vcc, v4, v3
	s_nop 1
	v_cndmask_b32_e32 v2, v2, v5, vcc
	v_sub_u32_e32 v5, v4, v3
	v_cndmask_b32_e32 v4, v4, v5, vcc
	v_add_u32_e32 v5, 1, v2
	v_cmp_ge_u32_e32 vcc, v4, v3
	v_add_u32_e32 v4, 1, v6
	s_nop 0
	v_cndmask_b32_e32 v2, v2, v5, vcc
	v_mul_lo_u32 v5, v3, v2
	v_readfirstlane_b32 s98, v2
	v_add_u32_e32 v3, v5, v3
	v_cmp_ne_u32_e32 vcc, v4, v3
	s_and_saveexec_b64 s[8:9], vcc
	s_xor_b64 s[8:9], exec, s[8:9]
	s_cbranch_execz .LBB0_640
	buffer_inv sc1
	v_lshl_add_u32 v2, v2, 1, 1
	s_waitcnt lgkmcnt(0)
	v_mov_b32_e32 v1, 0x2000
	global_load_dword v1, v1, s[6:7] offset:1024 sc1
	s_add_u32 s14, s6, 0x2400
	s_addc_u32 s15, s7, 0
	s_waitcnt vmcnt(0)
	v_cmp_lt_u32_e32 vcc, v1, v2
	s_and_saveexec_b64 s[10:11], vcc
	s_cbranch_execz .LBB0_639
	s_add_u32 s12, s82, 0x4200
	s_addc_u32 s13, s83, 0
	s_mov_b32 s26, 1
	s_mov_b64 s[16:17], 0
	v_mov_b32_e32 v1, 0
	s_branch .LBB0_630

; __device__ __forceinline__ unsigned xb_ld(unsigned* p)              { return __hip_atomic_load(p, __ATOMIC_RELAXED, __HIP_MEMORY_SCOPE_AGENT); }
; #define XB_SPIN(cond, bar) do { unsigned _sp = 0; while (cond) { __builtin_amdgcn_s_sleep(1); \
;     if ((++_sp & 255u) == 0u) { if (xb_ld(&(bar)[XB_TMO])) break; if (_sp > XB_SPIN_CAP) { atomicAdd(&(bar)[XB_TMO], 1u); break; } } } } while (0)
; __device__ __forceinline__ void xcd_barrier(const XcdBarrier& b) {
;     ...
;             XB_SPIN(xb_ld(&bar[XB_XGEN(b.x)]) == gen, bar);
.LBB0_632:
	global_load_dword v3, v1, s[14:15] sc1
	s_add_i32 s26, s26, 1
	s_mov_b64 s[22:23], -1
	s_waitcnt vmcnt(0)
	v_cmp_ge_u32_e32 vcc, v3, v2
	s_orn2_b64 s[20:21], vcc, exec
	s_branch .LBB0_629

; __device__ __forceinline__ unsigned xb_ld(unsigned* p)              { return __hip_atomic_load(p, __ATOMIC_RELAXED, __HIP_MEMORY_SCOPE_AGENT); }
; __device__ __forceinline__ unsigned xb_add(unsigned* p, unsigned v) { return __hip_atomic_fetch_add(p, v, __ATOMIC_RELAXED, __HIP_MEMORY_SCOPE_AGENT); }
; #define XB_SPIN(cond, bar) do { unsigned _sp = 0; while (cond) { __builtin_amdgcn_s_sleep(1); \
;     if ((++_sp & 255u) == 0u) { if (xb_ld(&(bar)[XB_TMO])) break; if (_sp > XB_SPIN_CAP) { atomicAdd(&(bar)[XB_TMO], 1u); break; } } } } while (0)
; __device__ __forceinline__ void xcd_barrier(const XcdBarrier& b) {
;     ...
;             asm volatile("buffer_inv sc1" ::: "memory");
;             __builtin_amdgcn_fence(__ATOMIC_RELEASE, "agent");
;             asm volatile("s_waitcnt vmcnt(0)" ::: "memory");
;             const unsigned og = xb_add(&bar[XB_TOP], 1u);
;             const unsigned tg = og / nx;
;             if (og + 1u == (tg + 1u) * nx) xb_add(&bar[XB_TOPGEN], 1u);
;             else XB_SPIN(xb_ld(&bar[XB_TOPGEN]) == tg, bar);
;             asm volatile("" ::: "memory");
;             xb_add(&bar[XB_XGEN(b.x)], 1u);
;             asm volatile("" ::: "memory");
.LBB0_643:
	s_or_b64 exec, exec, s[10:11]
	v_cvt_f32_u32_e32 v4, v1
	s_waitcnt vmcnt(0)
	v_readfirstlane_b32 s8, v3
	s_add_u32 s10, s82, 0x7500
	s_addc_u32 s11, s83, 0
	v_rcp_iflag_f32_e32 v4, v4
	v_add_u32_e32 v2, s8, v2
	v_add_u32_e32 v5, 1, v2
	s_mov_b64 s[12:13], -1
	v_mul_f32_e32 v3, 0x4f7ffffe, v4
	v_cvt_u32_f32_e32 v3, v3
	v_sub_u32_e32 v4, 0, v1
	v_mul_lo_u32 v4, v4, v3
	v_mul_hi_u32 v4, v3, v4
	v_add_u32_e32 v3, v3, v4
	v_mul_hi_u32 v3, v2, v3
	v_mul_lo_u32 v4, v3, v1
	v_sub_u32_e32 v2, v2, v4
	v_add_u32_e32 v6, 1, v3
	v_cmp_ge_u32_e32 vcc, v2, v1
	v_sub_u32_e32 v4, v2, v1
	s_nop 0
	v_cndmask_b32_e32 v3, v3, v6, vcc
	v_cndmask_b32_e32 v2, v2, v4, vcc
	v_add_u32_e32 v4, 1, v3
	v_cmp_ge_u32_e32 vcc, v2, v1
	s_nop 1
	v_cndmask_b32_e32 v4, v3, v4, vcc
	v_mul_lo_u32 v2, v1, v4
	v_add_u32_e32 v1, v2, v1
	v_cmp_ne_u32_e32 vcc, v5, v1
	v_mov_b64_e32 v[2:3], s[10:11]
	s_and_saveexec_b64 s[8:9], vcc
	s_cbranch_execz .LBB0_655
	s_add_u32 s10, s6, 0x2400
	s_addc_u32 s11, s7, 0
	v_mov_b32_e32 v4, s98
	v_lshl_add_u32 v4, v4, 1, 1
	v_mov_b32_e32 v1, 0
	global_load_dword v2, v1, s[10:11] sc1
	s_mov_b64 s[16:17], 0
	s_waitcnt vmcnt(0)
	v_cmp_lt_u32_e32 vcc, v2, v4
	s_and_saveexec_b64 s[14:15], vcc
	s_cbranch_execz .LBB0_654
	s_add_u32 s12, s82, 0x4200
	s_addc_u32 s13, s83, 0
	s_mov_b32 s26, 1
	s_branch .LBB0_647

; __device__ __forceinline__ unsigned xb_ld(unsigned* p)              { return __hip_atomic_load(p, __ATOMIC_RELAXED, __HIP_MEMORY_SCOPE_AGENT); }
; #define XB_SPIN(cond, bar) do { unsigned _sp = 0; while (cond) { __builtin_amdgcn_s_sleep(1); \
;     if ((++_sp & 255u) == 0u) { if (xb_ld(&(bar)[XB_TMO])) break; if (_sp > XB_SPIN_CAP) { atomicAdd(&(bar)[XB_TMO], 1u); break; } } } } while (0)
; __device__ __forceinline__ void xcd_barrier(const XcdBarrier& b) {
;     ...
;             else XB_SPIN(xb_ld(&bar[XB_TOPGEN]) == tg, bar);
.LBB0_649:
	global_load_dword v2, v1, s[10:11] sc1
	s_add_i32 s26, s26, 1
	s_mov_b64 s[20:21], -1
	s_waitcnt vmcnt(0)
	v_cmp_ge_u32_e32 vcc, v2, v4
	s_orn2_b64 s[24:25], vcc, exec
	s_branch .LBB0_646

; __device__ __forceinline__ unsigned xb_ld(unsigned* p)              { return __hip_atomic_load(p, __ATOMIC_RELAXED, __HIP_MEMORY_SCOPE_AGENT); }
; __device__ __forceinline__ unsigned xb_add(unsigned* p, unsigned v) { return __hip_atomic_fetch_add(p, v, __ATOMIC_RELAXED, __HIP_MEMORY_SCOPE_AGENT); }
; #define XB_SPIN(cond, bar) do { unsigned _sp = 0; while (cond) { __builtin_amdgcn_s_sleep(1); \
;     if ((++_sp & 255u) == 0u) { if (xb_ld(&(bar)[XB_TMO])) break; if (_sp > XB_SPIN_CAP) { atomicAdd(&(bar)[XB_TMO], 1u); break; } } } } while (0)
; __device__ __forceinline__ void xcd_barrier(const XcdBarrier& b) {
;     ...
;         const unsigned old = xb_add(&bar[XB_XSUB(b.x)], 1u);
;         const unsigned gen = old / nloc;
;         if (old + 1u == (gen + 1u) * nloc) {
;             asm volatile("buffer_inv sc1" ::: "memory");
;             __builtin_amdgcn_fence(__ATOMIC_RELEASE, "agent");
;             asm volatile("s_waitcnt vmcnt(0)" ::: "memory");
;             const unsigned og = xb_add(&bar[XB_TOP], 1u);
;             const unsigned tg = og / nx;
;             if (og + 1u == (tg + 1u) * nx) xb_add(&bar[XB_TOPGEN], 1u);
;             else XB_SPIN(xb_ld(&bar[XB_TOPGEN]) == tg, bar);
;             asm volatile("" ::: "memory");
;             xb_add(&bar[XB_XGEN(b.x)], 1u);
;             asm volatile("" ::: "memory");
;         } else {
;             asm volatile("buffer_inv sc1" ::: "memory");
;             XB_SPIN(xb_ld(&bar[XB_XGEN(b.x)]) == gen, bar);
;             asm volatile("" ::: "memory");
;             asm volatile("s_waitcnt vmcnt(0)" ::: "memory");
;         }
.LBB0_907:
	s_or_b64 exec, exec, s[10:11]
	v_cvt_f32_u32_e32 v5, v3
	s_waitcnt vmcnt(0)
	v_readfirstlane_b32 s8, v4
	v_sub_u32_e32 v4, 0, v3
	v_rcp_iflag_f32_e32 v5, v5
	v_add_u32_e32 v6, s8, v2
	v_mul_f32_e32 v5, 0x4f7ffffe, v5
	v_cvt_u32_f32_e32 v5, v5
	v_mul_lo_u32 v2, v4, v5
	v_mul_hi_u32 v2, v5, v2
	v_add_u32_e32 v2, v5, v2
	v_mul_hi_u32 v2, v6, v2
	v_mul_lo_u32 v4, v2, v3
	v_sub_u32_e32 v4, v6, v4
	v_add_u32_e32 v5, 1, v2
	v_cmp_ge_u32_e32 vcc, v4, v3
	s_nop 1
	v_cndmask_b32_e32 v2, v2, v5, vcc
	v_sub_u32_e32 v5, v4, v3
	v_cndmask_b32_e32 v4, v4, v5, vcc
	v_add_u32_e32 v5, 1, v2
	v_cmp_ge_u32_e32 vcc, v4, v3
	v_add_u32_e32 v4, 1, v6
	s_nop 0
	v_cndmask_b32_e32 v2, v2, v5, vcc
	v_mul_lo_u32 v5, v3, v2
	v_readfirstlane_b32 s98, v2
	v_add_u32_e32 v3, v5, v3
	v_cmp_ne_u32_e32 vcc, v4, v3
	s_and_saveexec_b64 s[8:9], vcc
	s_xor_b64 s[8:9], exec, s[8:9]
	s_cbranch_execz .LBB0_921
	buffer_inv sc1
	v_lshl_add_u32 v2, v2, 1, 1
	s_waitcnt lgkmcnt(0)
	v_mov_b32_e32 v1, 0x2000
	global_load_dword v1, v1, s[4:5] offset:1024 sc1
	s_add_u32 s14, s4, 0x2400
	s_addc_u32 s15, s5, 0
	s_waitcnt vmcnt(0)
	v_cmp_lt_u32_e32 vcc, v1, v2
	s_and_saveexec_b64 s[10:11], vcc
	s_cbranch_execz .LBB0_920
	s_add_u32 s12, s82, 0x4200
	s_addc_u32 s13, s83, 0
	s_mov_b32 s26, 1
	s_mov_b64 s[16:17], 0
	v_mov_b32_e32 v1, 0
	s_branch .LBB0_911

; __device__ __forceinline__ unsigned xb_ld(unsigned* p)              { return __hip_atomic_load(p, __ATOMIC_RELAXED, __HIP_MEMORY_SCOPE_AGENT); }
; __device__ __forceinline__ unsigned xb_add(unsigned* p, unsigned v) { return __hip_atomic_fetch_add(p, v, __ATOMIC_RELAXED, __HIP_MEMORY_SCOPE_AGENT); }
; #define XB_SPIN(cond, bar) do { unsigned _sp = 0; while (cond) { __builtin_amdgcn_s_sleep(1); \
;     if ((++_sp & 255u) == 0u) { if (xb_ld(&(bar)[XB_TMO])) break; if (_sp > XB_SPIN_CAP) { atomicAdd(&(bar)[XB_TMO], 1u); break; } } } } while (0)
; __device__ __forceinline__ void xcd_barrier(const XcdBarrier& b) {
;     ...
;             asm volatile("buffer_inv sc1" ::: "memory");
;             __builtin_amdgcn_fence(__ATOMIC_RELEASE, "agent");
;             asm volatile("s_waitcnt vmcnt(0)" ::: "memory");
;             const unsigned og = xb_add(&bar[XB_TOP], 1u);
;             const unsigned tg = og / nx;
;             if (og + 1u == (tg + 1u) * nx) xb_add(&bar[XB_TOPGEN], 1u);
;             else XB_SPIN(xb_ld(&bar[XB_TOPGEN]) == tg, bar);
;             asm volatile("" ::: "memory");
;             xb_add(&bar[XB_XGEN(b.x)], 1u);
;             asm volatile("" ::: "memory");
.LBB0_924:
	s_or_b64 exec, exec, s[10:11]
	v_cvt_f32_u32_e32 v4, v1
	s_waitcnt vmcnt(0)
	v_readfirstlane_b32 s8, v3
	s_add_u32 s10, s82, 0x7500
	s_addc_u32 s11, s83, 0
	v_rcp_iflag_f32_e32 v4, v4
	v_add_u32_e32 v2, s8, v2
	v_add_u32_e32 v5, 1, v2
	s_mov_b64 s[12:13], -1
	v_mul_f32_e32 v3, 0x4f7ffffe, v4
	v_cvt_u32_f32_e32 v3, v3
	v_sub_u32_e32 v4, 0, v1
	v_mul_lo_u32 v4, v4, v3
	v_mul_hi_u32 v4, v3, v4
	v_add_u32_e32 v3, v3, v4
	v_mul_hi_u32 v3, v2, v3
	v_mul_lo_u32 v4, v3, v1
	v_sub_u32_e32 v2, v2, v4
	v_add_u32_e32 v6, 1, v3
	v_cmp_ge_u32_e32 vcc, v2, v1
	v_sub_u32_e32 v4, v2, v1
	s_nop 0
	v_cndmask_b32_e32 v3, v3, v6, vcc
	v_cndmask_b32_e32 v2, v2, v4, vcc
	v_add_u32_e32 v4, 1, v3
	v_cmp_ge_u32_e32 vcc, v2, v1
	s_nop 1
	v_cndmask_b32_e32 v4, v3, v4, vcc
	v_mul_lo_u32 v2, v1, v4
	v_add_u32_e32 v1, v2, v1
	v_cmp_ne_u32_e32 vcc, v5, v1
	v_mov_b64_e32 v[2:3], s[10:11]
	s_and_saveexec_b64 s[8:9], vcc
	s_cbranch_execz .LBB0_936
	s_add_u32 s10, s4, 0x2400
	s_addc_u32 s11, s5, 0
	v_mov_b32_e32 v4, s98
	v_lshl_add_u32 v4, v4, 1, 1
	v_mov_b32_e32 v1, 0
	global_load_dword v2, v1, s[10:11] sc1
	s_mov_b64 s[16:17], 0
	s_waitcnt vmcnt(0)
	v_cmp_lt_u32_e32 vcc, v2, v4
	s_and_saveexec_b64 s[14:15], vcc
	s_cbranch_execz .LBB0_935
	s_add_u32 s12, s82, 0x4200
	s_addc_u32 s13, s83, 0
	s_mov_b32 s26, 1
	s_branch .LBB0_928

; __device__ __forceinline__ unsigned xb_ld(unsigned* p)              { return __hip_atomic_load(p, __ATOMIC_RELAXED, __HIP_MEMORY_SCOPE_AGENT); }
; __device__ __forceinline__ unsigned xb_add(unsigned* p, unsigned v) { return __hip_atomic_fetch_add(p, v, __ATOMIC_RELAXED, __HIP_MEMORY_SCOPE_AGENT); }
; #define XB_SPIN(cond, bar) do { unsigned _sp = 0; while (cond) { __builtin_amdgcn_s_sleep(1); \
;     if ((++_sp & 255u) == 0u) { if (xb_ld(&(bar)[XB_TMO])) break; if (_sp > XB_SPIN_CAP) { atomicAdd(&(bar)[XB_TMO], 1u); break; } } } } while (0)
; __device__ __forceinline__ void xcd_barrier(const XcdBarrier& b) {
;     ...
;         const unsigned old = xb_add(&bar[XB_XSUB(b.x)], 1u);
;         const unsigned gen = old / nloc;
;         if (old + 1u == (gen + 1u) * nloc) {
;             asm volatile("buffer_inv sc1" ::: "memory");
;             __builtin_amdgcn_fence(__ATOMIC_RELEASE, "agent");
;             asm volatile("s_waitcnt vmcnt(0)" ::: "memory");
;             const unsigned og = xb_add(&bar[XB_TOP], 1u);
;             const unsigned tg = og / nx;
;             if (og + 1u == (tg + 1u) * nx) xb_add(&bar[XB_TOPGEN], 1u);
;             else XB_SPIN(xb_ld(&bar[XB_TOPGEN]) == tg, bar);
;             asm volatile("" ::: "memory");
;             xb_add(&bar[XB_XGEN(b.x)], 1u);
;             asm volatile("" ::: "memory");
;         } else {
;             asm volatile("buffer_inv sc1" ::: "memory");
;             XB_SPIN(xb_ld(&bar[XB_XGEN(b.x)]) == gen, bar);
;             asm volatile("" ::: "memory");
;             asm volatile("s_waitcnt vmcnt(0)" ::: "memory");
;         }
.LBB0_1020:
	s_or_b64 exec, exec, s[12:13]
	v_cvt_f32_u32_e32 v5, v3
	s_waitcnt vmcnt(0)
	v_readfirstlane_b32 s10, v4
	v_sub_u32_e32 v4, 0, v3
	v_rcp_iflag_f32_e32 v5, v5
	v_add_u32_e32 v6, s10, v2
	v_mul_f32_e32 v5, 0x4f7ffffe, v5
	v_cvt_u32_f32_e32 v5, v5
	v_mul_lo_u32 v2, v4, v5
	v_mul_hi_u32 v2, v5, v2
	v_add_u32_e32 v2, v5, v2
	v_mul_hi_u32 v2, v6, v2
	v_mul_lo_u32 v4, v2, v3
	v_sub_u32_e32 v4, v6, v4
	v_add_u32_e32 v5, 1, v2
	v_cmp_ge_u32_e32 vcc, v4, v3
	s_nop 1
	v_cndmask_b32_e32 v2, v2, v5, vcc
	v_sub_u32_e32 v5, v4, v3
	v_cndmask_b32_e32 v4, v4, v5, vcc
	v_add_u32_e32 v5, 1, v2
	v_cmp_ge_u32_e32 vcc, v4, v3
	v_add_u32_e32 v4, 1, v6
	s_nop 0
	v_cndmask_b32_e32 v2, v2, v5, vcc
	v_mul_lo_u32 v5, v3, v2
	v_readfirstlane_b32 s98, v2
	v_add_u32_e32 v3, v5, v3
	v_cmp_ne_u32_e32 vcc, v4, v3
	s_and_saveexec_b64 s[10:11], vcc
	s_xor_b64 s[10:11], exec, s[10:11]
	s_cbranch_execz .LBB0_1034
	buffer_inv sc1
	v_lshl_add_u32 v2, v2, 1, 1
	s_waitcnt lgkmcnt(0)
	v_mov_b32_e32 v1, 0x2000
	global_load_dword v1, v1, s[8:9] offset:1024 sc1
	s_add_u32 s16, s8, 0x2400
	s_addc_u32 s17, s9, 0
	s_waitcnt vmcnt(0)
	v_cmp_lt_u32_e32 vcc, v1, v2
	s_and_saveexec_b64 s[12:13], vcc
	s_cbranch_execz .LBB0_1033
	s_add_u32 s14, s82, 0x4200
	s_addc_u32 s15, s83, 0
	s_mov_b32 s28, 1
	s_mov_b64 s[18:19], 0
	v_mov_b32_e32 v1, 0
	s_branch .LBB0_1024

; __device__ __forceinline__ unsigned xb_ld(unsigned* p)              { return __hip_atomic_load(p, __ATOMIC_RELAXED, __HIP_MEMORY_SCOPE_AGENT); }
; __device__ __forceinline__ unsigned xb_add(unsigned* p, unsigned v) { return __hip_atomic_fetch_add(p, v, __ATOMIC_RELAXED, __HIP_MEMORY_SCOPE_AGENT); }
; #define XB_SPIN(cond, bar) do { unsigned _sp = 0; while (cond) { __builtin_amdgcn_s_sleep(1); \
;     if ((++_sp & 255u) == 0u) { if (xb_ld(&(bar)[XB_TMO])) break; if (_sp > XB_SPIN_CAP) { atomicAdd(&(bar)[XB_TMO], 1u); break; } } } } while (0)
; __device__ __forceinline__ void xcd_barrier(const XcdBarrier& b) {
;     ...
;             asm volatile("buffer_inv sc1" ::: "memory");
;             __builtin_amdgcn_fence(__ATOMIC_RELEASE, "agent");
;             asm volatile("s_waitcnt vmcnt(0)" ::: "memory");
;             const unsigned og = xb_add(&bar[XB_TOP], 1u);
;             const unsigned tg = og / nx;
;             if (og + 1u == (tg + 1u) * nx) xb_add(&bar[XB_TOPGEN], 1u);
;             else XB_SPIN(xb_ld(&bar[XB_TOPGEN]) == tg, bar);
;             asm volatile("" ::: "memory");
;             xb_add(&bar[XB_XGEN(b.x)], 1u);
;             asm volatile("" ::: "memory");
.LBB0_1037:
	s_or_b64 exec, exec, s[12:13]
	v_cvt_f32_u32_e32 v4, v1
	s_waitcnt vmcnt(0)
	v_readfirstlane_b32 s10, v3
	s_add_u32 s12, s82, 0x7500
	s_addc_u32 s13, s83, 0
	v_rcp_iflag_f32_e32 v4, v4
	v_add_u32_e32 v2, s10, v2
	v_add_u32_e32 v5, 1, v2
	s_mov_b64 s[14:15], -1
	v_mul_f32_e32 v3, 0x4f7ffffe, v4
	v_cvt_u32_f32_e32 v3, v3
	v_sub_u32_e32 v4, 0, v1
	v_mul_lo_u32 v4, v4, v3
	v_mul_hi_u32 v4, v3, v4
	v_add_u32_e32 v3, v3, v4
	v_mul_hi_u32 v3, v2, v3
	v_mul_lo_u32 v4, v3, v1
	v_sub_u32_e32 v2, v2, v4
	v_add_u32_e32 v6, 1, v3
	v_cmp_ge_u32_e32 vcc, v2, v1
	v_sub_u32_e32 v4, v2, v1
	s_nop 0
	v_cndmask_b32_e32 v3, v3, v6, vcc
	v_cndmask_b32_e32 v2, v2, v4, vcc
	v_add_u32_e32 v4, 1, v3
	v_cmp_ge_u32_e32 vcc, v2, v1
	s_nop 1
	v_cndmask_b32_e32 v4, v3, v4, vcc
	v_mul_lo_u32 v2, v1, v4
	v_add_u32_e32 v1, v2, v1
	v_cmp_ne_u32_e32 vcc, v5, v1
	v_mov_b64_e32 v[2:3], s[12:13]
	s_and_saveexec_b64 s[10:11], vcc
	s_cbranch_execz .LBB0_1049
	s_add_u32 s12, s8, 0x2400
	s_addc_u32 s13, s9, 0
	v_mov_b32_e32 v4, s98
	v_lshl_add_u32 v4, v4, 1, 1
	v_mov_b32_e32 v1, 0
	global_load_dword v2, v1, s[12:13] sc1
	s_mov_b64 s[18:19], 0
	s_waitcnt vmcnt(0)
	v_cmp_lt_u32_e32 vcc, v2, v4
	s_and_saveexec_b64 s[16:17], vcc
	s_cbranch_execz .LBB0_1048
	s_add_u32 s14, s82, 0x4200
	s_addc_u32 s15, s83, 0
	s_mov_b32 s28, 1
	s_branch .LBB0_1041

; __device__ __forceinline__ unsigned xb_ld(unsigned* p)              { return __hip_atomic_load(p, __ATOMIC_RELAXED, __HIP_MEMORY_SCOPE_AGENT); }
; #define XB_SPIN(cond, bar) do { unsigned _sp = 0; while (cond) { __builtin_amdgcn_s_sleep(1); \
;     if ((++_sp & 255u) == 0u) { if (xb_ld(&(bar)[XB_TMO])) break; if (_sp > XB_SPIN_CAP) { atomicAdd(&(bar)[XB_TMO], 1u); break; } } } } while (0)
; __device__ __forceinline__ void xcd_barrier(const XcdBarrier& b) {
;     ...
;             else XB_SPIN(xb_ld(&bar[XB_TOPGEN]) == tg, bar);
.LBB0_1043:
	global_load_dword v2, v1, s[12:13] sc1
	s_add_i32 s28, s28, 1
	s_mov_b64 s[22:23], -1
	s_waitcnt vmcnt(0)
	v_cmp_ge_u32_e32 vcc, v2, v4
	s_orn2_b64 s[26:27], vcc, exec
	s_branch .LBB0_1040

; __device__ __forceinline__ unsigned xb_ld(unsigned* p)              { return __hip_atomic_load(p, __ATOMIC_RELAXED, __HIP_MEMORY_SCOPE_AGENT); }
; __device__ __forceinline__ unsigned xb_add(unsigned* p, unsigned v) { return __hip_atomic_fetch_add(p, v, __ATOMIC_RELAXED, __HIP_MEMORY_SCOPE_AGENT); }
; #define XB_SPIN(cond, bar) do { unsigned _sp = 0; while (cond) { __builtin_amdgcn_s_sleep(1); \
;     if ((++_sp & 255u) == 0u) { if (xb_ld(&(bar)[XB_TMO])) break; if (_sp > XB_SPIN_CAP) { atomicAdd(&(bar)[XB_TMO], 1u); break; } } } } while (0)
; __device__ __forceinline__ void xcd_barrier(const XcdBarrier& b) {
;     ...
;             const unsigned og = xb_add(&bar[XB_TOP], 1u);
;             const unsigned tg = og / nx;
;             if (og + 1u == (tg + 1u) * nx) xb_add(&bar[XB_TOPGEN], 1u);
;             else XB_SPIN(xb_ld(&bar[XB_TOPGEN]) == tg, bar);
;             asm volatile("" ::: "memory");
;             xb_add(&bar[XB_XGEN(b.x)], 1u);
.LBB0_1049:
	s_or_b64 exec, exec, s[10:11]
	s_and_saveexec_b64 s[10:11], s[14:15]
	s_cbranch_execz .LBB0_1051
	v_mov_b32_e32 v1, 1
	global_atomic_add v[2:3], v1, off
	v_mov_b32_e32 v4, 0x6400
	global_atomic_add v4, v1, s[82:83]
	global_atomic_add v4, v1, s[82:83] offset:256
	global_atomic_add v4, v1, s[82:83] offset:512
	global_atomic_add v4, v1, s[82:83] offset:768
	global_atomic_add v4, v1, s[82:83] offset:1024
	global_atomic_add v4, v1, s[82:83] offset:1280
	global_atomic_add v4, v1, s[82:83] offset:1536
	global_atomic_add v4, v1, s[82:83] offset:1792
	global_atomic_add v4, v1, s[82:83] offset:2048
	global_atomic_add v4, v1, s[82:83] offset:2304
	global_atomic_add v4, v1, s[82:83] offset:2560
	global_atomic_add v4, v1, s[82:83] offset:2816
	global_atomic_add v4, v1, s[82:83] offset:3072
	global_atomic_add v4, v1, s[82:83] offset:3328
	global_atomic_add v4, v1, s[82:83] offset:3584
	global_atomic_add v4, v1, s[82:83] offset:3840

; __device__ __forceinline__ unsigned xb_ld(unsigned* p)              { return __hip_atomic_load(p, __ATOMIC_RELAXED, __HIP_MEMORY_SCOPE_AGENT); }
; __device__ __forceinline__ unsigned xb_add(unsigned* p, unsigned v) { return __hip_atomic_fetch_add(p, v, __ATOMIC_RELAXED, __HIP_MEMORY_SCOPE_AGENT); }
; #define XB_SPIN(cond, bar) do { unsigned _sp = 0; while (cond) { __builtin_amdgcn_s_sleep(1); \
;     if ((++_sp & 255u) == 0u) { if (xb_ld(&(bar)[XB_TMO])) break; if (_sp > XB_SPIN_CAP) { atomicAdd(&(bar)[XB_TMO], 1u); break; } } } } while (0)
; __device__ __forceinline__ void xcd_barrier(const XcdBarrier& b) {
;     ...
;         const unsigned old = xb_add(&bar[XB_XSUB(b.x)], 1u);
;         const unsigned gen = old / nloc;
;         if (old + 1u == (gen + 1u) * nloc) {
;             asm volatile("buffer_inv sc1" ::: "memory");
;             __builtin_amdgcn_fence(__ATOMIC_RELEASE, "agent");
;             asm volatile("s_waitcnt vmcnt(0)" ::: "memory");
;             const unsigned og = xb_add(&bar[XB_TOP], 1u);
;             const unsigned tg = og / nx;
;             if (og + 1u == (tg + 1u) * nx) xb_add(&bar[XB_TOPGEN], 1u);
;             else XB_SPIN(xb_ld(&bar[XB_TOPGEN]) == tg, bar);
;             asm volatile("" ::: "memory");
;             xb_add(&bar[XB_XGEN(b.x)], 1u);
;             asm volatile("" ::: "memory");
;         } else {
;             asm volatile("buffer_inv sc1" ::: "memory");
;             XB_SPIN(xb_ld(&bar[XB_XGEN(b.x)]) == gen, bar);
;             asm volatile("" ::: "memory");
;             asm volatile("s_waitcnt vmcnt(0)" ::: "memory");
;         }
.LBB0_1228:
	s_or_b64 exec, exec, s[14:15]
	v_cvt_f32_u32_e32 v5, v3
	s_waitcnt vmcnt(0)
	v_readfirstlane_b32 s12, v4
	v_sub_u32_e32 v4, 0, v3
	v_rcp_iflag_f32_e32 v5, v5
	v_add_u32_e32 v6, s12, v2
	v_mul_f32_e32 v5, 0x4f7ffffe, v5
	v_cvt_u32_f32_e32 v5, v5
	v_mul_lo_u32 v2, v4, v5
	v_mul_hi_u32 v2, v5, v2
	v_add_u32_e32 v2, v5, v2
	v_mul_hi_u32 v2, v6, v2
	v_mul_lo_u32 v4, v2, v3
	v_sub_u32_e32 v4, v6, v4
	v_add_u32_e32 v5, 1, v2
	v_cmp_ge_u32_e32 vcc, v4, v3
	s_nop 1
	v_cndmask_b32_e32 v2, v2, v5, vcc
	v_sub_u32_e32 v5, v4, v3
	v_cndmask_b32_e32 v4, v4, v5, vcc
	v_add_u32_e32 v5, 1, v2
	v_cmp_ge_u32_e32 vcc, v4, v3
	v_add_u32_e32 v4, 1, v6
	s_nop 0
	v_cndmask_b32_e32 v2, v2, v5, vcc
	v_mul_lo_u32 v5, v3, v2
	v_readfirstlane_b32 s98, v2
	v_add_u32_e32 v3, v5, v3
	v_cmp_ne_u32_e32 vcc, v4, v3
	s_and_saveexec_b64 s[12:13], vcc
	s_xor_b64 s[12:13], exec, s[12:13]
	s_cbranch_execz .LBB0_1242
	buffer_inv sc1
	v_lshl_add_u32 v2, v2, 1, 1
	s_waitcnt lgkmcnt(0)
	v_mov_b32_e32 v1, 0x2000
	global_load_dword v1, v1, s[10:11] offset:1024 sc1
	s_add_u32 s18, s10, 0x2400
	s_addc_u32 s19, s11, 0
	s_waitcnt vmcnt(0)
	v_cmp_lt_u32_e32 vcc, v1, v2
	s_and_saveexec_b64 s[14:15], vcc
	s_cbranch_execz .LBB0_1241
	s_add_u32 s16, s82, 0x4200
	s_addc_u32 s17, s83, 0
	s_mov_b32 s30, 1
	s_mov_b64 s[20:21], 0
	v_mov_b32_e32 v1, 0
	s_branch .LBB0_1232

; __device__ __forceinline__ unsigned xb_ld(unsigned* p)              { return __hip_atomic_load(p, __ATOMIC_RELAXED, __HIP_MEMORY_SCOPE_AGENT); }
; #define XB_SPIN(cond, bar) do { unsigned _sp = 0; while (cond) { __builtin_amdgcn_s_sleep(1); \
;     if ((++_sp & 255u) == 0u) { if (xb_ld(&(bar)[XB_TMO])) break; if (_sp > XB_SPIN_CAP) { atomicAdd(&(bar)[XB_TMO], 1u); break; } } } } while (0)
; __device__ __forceinline__ void xcd_barrier(const XcdBarrier& b) {
;     ...
;             XB_SPIN(xb_ld(&bar[XB_XGEN(b.x)]) == gen, bar);
.LBB0_1234:
	global_load_dword v3, v1, s[18:19] sc1
	s_add_i32 s30, s30, 1
	s_mov_b64 s[26:27], -1
	s_waitcnt vmcnt(0)
	v_cmp_ge_u32_e32 vcc, v3, v2
	s_orn2_b64 s[24:25], vcc, exec
	s_branch .LBB0_1231

; __device__ __forceinline__ unsigned xb_ld(unsigned* p)              { return __hip_atomic_load(p, __ATOMIC_RELAXED, __HIP_MEMORY_SCOPE_AGENT); }
; __device__ __forceinline__ unsigned xb_add(unsigned* p, unsigned v) { return __hip_atomic_fetch_add(p, v, __ATOMIC_RELAXED, __HIP_MEMORY_SCOPE_AGENT); }
; #define XB_SPIN(cond, bar) do { unsigned _sp = 0; while (cond) { __builtin_amdgcn_s_sleep(1); \
;     if ((++_sp & 255u) == 0u) { if (xb_ld(&(bar)[XB_TMO])) break; if (_sp > XB_SPIN_CAP) { atomicAdd(&(bar)[XB_TMO], 1u); break; } } } } while (0)
; __device__ __forceinline__ void xcd_barrier(const XcdBarrier& b) {
;     ...
;             asm volatile("buffer_inv sc1" ::: "memory");
;             __builtin_amdgcn_fence(__ATOMIC_RELEASE, "agent");
;             asm volatile("s_waitcnt vmcnt(0)" ::: "memory");
;             const unsigned og = xb_add(&bar[XB_TOP], 1u);
;             const unsigned tg = og / nx;
;             if (og + 1u == (tg + 1u) * nx) xb_add(&bar[XB_TOPGEN], 1u);
;             else XB_SPIN(xb_ld(&bar[XB_TOPGEN]) == tg, bar);
;             asm volatile("" ::: "memory");
;             xb_add(&bar[XB_XGEN(b.x)], 1u);
;             asm volatile("" ::: "memory");
.LBB0_1245:
	s_or_b64 exec, exec, s[14:15]
	v_cvt_f32_u32_e32 v4, v1
	s_waitcnt vmcnt(0)
	v_readfirstlane_b32 s12, v3
	s_add_u32 s14, s82, 0x7500
	s_addc_u32 s15, s83, 0
	v_rcp_iflag_f32_e32 v4, v4
	v_add_u32_e32 v2, s12, v2
	v_add_u32_e32 v5, 1, v2
	s_mov_b64 s[16:17], -1
	v_mul_f32_e32 v3, 0x4f7ffffe, v4
	v_cvt_u32_f32_e32 v3, v3
	v_sub_u32_e32 v4, 0, v1
	v_mul_lo_u32 v4, v4, v3
	v_mul_hi_u32 v4, v3, v4
	v_add_u32_e32 v3, v3, v4
	v_mul_hi_u32 v3, v2, v3
	v_mul_lo_u32 v4, v3, v1
	v_sub_u32_e32 v2, v2, v4
	v_add_u32_e32 v6, 1, v3
	v_cmp_ge_u32_e32 vcc, v2, v1
	v_sub_u32_e32 v4, v2, v1
	s_nop 0
	v_cndmask_b32_e32 v3, v3, v6, vcc
	v_cndmask_b32_e32 v2, v2, v4, vcc
	v_add_u32_e32 v4, 1, v3
	v_cmp_ge_u32_e32 vcc, v2, v1
	s_nop 1
	v_cndmask_b32_e32 v4, v3, v4, vcc
	v_mul_lo_u32 v2, v1, v4
	v_add_u32_e32 v1, v2, v1
	v_cmp_ne_u32_e32 vcc, v5, v1
	v_mov_b64_e32 v[2:3], s[14:15]
	s_and_saveexec_b64 s[12:13], vcc
	s_cbranch_execz .LBB0_1257
	s_add_u32 s14, s10, 0x2400
	s_addc_u32 s15, s11, 0
	v_mov_b32_e32 v4, s98
	v_lshl_add_u32 v4, v4, 1, 1
	v_mov_b32_e32 v1, 0
	global_load_dword v2, v1, s[14:15] sc1
	s_mov_b64 s[20:21], 0
	s_waitcnt vmcnt(0)
	v_cmp_lt_u32_e32 vcc, v2, v4
	s_and_saveexec_b64 s[18:19], vcc
	s_cbranch_execz .LBB0_1256
	s_add_u32 s16, s82, 0x4200
	s_addc_u32 s17, s83, 0
	s_mov_b32 s30, 1
	s_branch .LBB0_1249

; __device__ __forceinline__ unsigned xb_ld(unsigned* p)              { return __hip_atomic_load(p, __ATOMIC_RELAXED, __HIP_MEMORY_SCOPE_AGENT); }
; #define XB_SPIN(cond, bar) do { unsigned _sp = 0; while (cond) { __builtin_amdgcn_s_sleep(1); \
;     if ((++_sp & 255u) == 0u) { if (xb_ld(&(bar)[XB_TMO])) break; if (_sp > XB_SPIN_CAP) { atomicAdd(&(bar)[XB_TMO], 1u); break; } } } } while (0)
; __device__ __forceinline__ void xcd_barrier(const XcdBarrier& b) {
;     ...
;             else XB_SPIN(xb_ld(&bar[XB_TOPGEN]) == tg, bar);
.LBB0_1251:
	global_load_dword v2, v1, s[14:15] sc1
	s_add_i32 s30, s30, 1
	s_mov_b64 s[24:25], -1
	s_waitcnt vmcnt(0)
	v_cmp_ge_u32_e32 vcc, v2, v4
	s_orn2_b64 s[28:29], vcc, exec
	s_branch .LBB0_1248

; __device__ __forceinline__ unsigned xb_ld(unsigned* p)              { return __hip_atomic_load(p, __ATOMIC_RELAXED, __HIP_MEMORY_SCOPE_AGENT); }
; __device__ __forceinline__ unsigned xb_add(unsigned* p, unsigned v) { return __hip_atomic_fetch_add(p, v, __ATOMIC_RELAXED, __HIP_MEMORY_SCOPE_AGENT); }
; #define XB_SPIN(cond, bar) do { unsigned _sp = 0; while (cond) { __builtin_amdgcn_s_sleep(1); \
;     if ((++_sp & 255u) == 0u) { if (xb_ld(&(bar)[XB_TMO])) break; if (_sp > XB_SPIN_CAP) { atomicAdd(&(bar)[XB_TMO], 1u); break; } } } } while (0)
; __device__ __forceinline__ void xcd_barrier(const XcdBarrier& b) {
;     ...
;             const unsigned og = xb_add(&bar[XB_TOP], 1u);
;             const unsigned tg = og / nx;
;             if (og + 1u == (tg + 1u) * nx) xb_add(&bar[XB_TOPGEN], 1u);
;             else XB_SPIN(xb_ld(&bar[XB_TOPGEN]) == tg, bar);
;             asm volatile("" ::: "memory");
;             xb_add(&bar[XB_XGEN(b.x)], 1u);
.LBB0_1257:
	s_or_b64 exec, exec, s[12:13]
	s_and_saveexec_b64 s[12:13], s[16:17]
	s_cbranch_execz .LBB0_1259
	v_mov_b32_e32 v1, 1
	global_atomic_add v[2:3], v1, off
	v_mov_b32_e32 v4, 0x6400
	global_atomic_add v4, v1, s[82:83]
	global_atomic_add v4, v1, s[82:83] offset:256
	global_atomic_add v4, v1, s[82:83] offset:512
	global_atomic_add v4, v1, s[82:83] offset:768
	global_atomic_add v4, v1, s[82:83] offset:1024
	global_atomic_add v4, v1, s[82:83] offset:1280
	global_atomic_add v4, v1, s[82:83] offset:1536
	global_atomic_add v4, v1, s[82:83] offset:1792
	global_atomic_add v4, v1, s[82:83] offset:2048
	global_atomic_add v4, v1, s[82:83] offset:2304
	global_atomic_add v4, v1, s[82:83] offset:2560
	global_atomic_add v4, v1, s[82:83] offset:2816
	global_atomic_add v4, v1, s[82:83] offset:3072
	global_atomic_add v4, v1, s[82:83] offset:3328
	global_atomic_add v4, v1, s[82:83] offset:3584
	global_atomic_add v4, v1, s[82:83] offset:3840

; __device__ __forceinline__ unsigned xb_ld(unsigned* p)              { return __hip_atomic_load(p, __ATOMIC_RELAXED, __HIP_MEMORY_SCOPE_AGENT); }
; __device__ __forceinline__ unsigned xb_add(unsigned* p, unsigned v) { return __hip_atomic_fetch_add(p, v, __ATOMIC_RELAXED, __HIP_MEMORY_SCOPE_AGENT); }
; #define XB_SPIN(cond, bar) do { unsigned _sp = 0; while (cond) { __builtin_amdgcn_s_sleep(1); \
;     if ((++_sp & 255u) == 0u) { if (xb_ld(&(bar)[XB_TMO])) break; if (_sp > XB_SPIN_CAP) { atomicAdd(&(bar)[XB_TMO], 1u); break; } } } } while (0)
; __device__ __forceinline__ void xcd_barrier(const XcdBarrier& b) {
;     ...
;         const unsigned old = xb_add(&bar[XB_XSUB(b.x)], 1u);
;         const unsigned gen = old / nloc;
;         if (old + 1u == (gen + 1u) * nloc) {
;             asm volatile("buffer_inv sc1" ::: "memory");
;             __builtin_amdgcn_fence(__ATOMIC_RELEASE, "agent");
;             asm volatile("s_waitcnt vmcnt(0)" ::: "memory");
;             const unsigned og = xb_add(&bar[XB_TOP], 1u);
;             const unsigned tg = og / nx;
;             if (og + 1u == (tg + 1u) * nx) xb_add(&bar[XB_TOPGEN], 1u);
;             else XB_SPIN(xb_ld(&bar[XB_TOPGEN]) == tg, bar);
;             asm volatile("" ::: "memory");
;             xb_add(&bar[XB_XGEN(b.x)], 1u);
;             asm volatile("" ::: "memory");
;         } else {
;             asm volatile("buffer_inv sc1" ::: "memory");
;             XB_SPIN(xb_ld(&bar[XB_XGEN(b.x)]) == gen, bar);
;             asm volatile("" ::: "memory");
;             asm volatile("s_waitcnt vmcnt(0)" ::: "memory");
;         }
.LBB0_1841:
	s_or_b64 exec, exec, s[12:13]
	v_cvt_f32_u32_e32 v5, v3
	s_waitcnt vmcnt(0)
	v_readfirstlane_b32 s3, v4
	v_sub_u32_e32 v4, 0, v3
	v_rcp_iflag_f32_e32 v5, v5
	v_add_u32_e32 v6, s3, v2
	v_mul_f32_e32 v5, 0x4f7ffffe, v5
	v_cvt_u32_f32_e32 v5, v5
	v_mul_lo_u32 v2, v4, v5
	v_mul_hi_u32 v2, v5, v2
	v_add_u32_e32 v2, v5, v2
	v_mul_hi_u32 v2, v6, v2
	v_mul_lo_u32 v4, v2, v3
	v_sub_u32_e32 v4, v6, v4
	v_add_u32_e32 v5, 1, v2
	v_cmp_ge_u32_e32 vcc, v4, v3
	s_nop 1
	v_cndmask_b32_e32 v2, v2, v5, vcc
	v_sub_u32_e32 v5, v4, v3
	v_cndmask_b32_e32 v4, v4, v5, vcc
	v_add_u32_e32 v5, 1, v2
	v_cmp_ge_u32_e32 vcc, v4, v3
	v_add_u32_e32 v4, 1, v6
	s_nop 0
	v_cndmask_b32_e32 v2, v2, v5, vcc
	v_mul_lo_u32 v5, v3, v2
	v_readfirstlane_b32 s98, v2
	v_add_u32_e32 v3, v5, v3
	v_cmp_ne_u32_e32 vcc, v4, v3
	s_and_saveexec_b64 s[10:11], vcc
	s_xor_b64 s[10:11], exec, s[10:11]
	s_cbranch_execz .LBB0_1855
	buffer_inv sc1
	v_lshl_add_u32 v2, v2, 1, 1
	s_waitcnt lgkmcnt(0)
	v_mov_b32_e32 v1, 0x2000
	global_load_dword v1, v1, s[8:9] offset:1024 sc1
	s_add_u32 s16, s8, 0x2400
	s_addc_u32 s17, s9, 0
	s_waitcnt vmcnt(0)
	v_cmp_lt_u32_e32 vcc, v1, v2
	s_and_saveexec_b64 s[12:13], vcc
	s_cbranch_execz .LBB0_1854
	s_add_u32 s14, s82, 0x4200
	s_addc_u32 s15, s83, 0
	s_mov_b32 s3, 1
	s_mov_b64 s[18:19], 0
	v_mov_b32_e32 v1, 0
	s_branch .LBB0_1845

; __device__ __forceinline__ unsigned xb_ld(unsigned* p)              { return __hip_atomic_load(p, __ATOMIC_RELAXED, __HIP_MEMORY_SCOPE_AGENT); }
; #define XB_SPIN(cond, bar) do { unsigned _sp = 0; while (cond) { __builtin_amdgcn_s_sleep(1); \
;     if ((++_sp & 255u) == 0u) { if (xb_ld(&(bar)[XB_TMO])) break; if (_sp > XB_SPIN_CAP) { atomicAdd(&(bar)[XB_TMO], 1u); break; } } } } while (0)
; __device__ __forceinline__ void xcd_barrier(const XcdBarrier& b) {
;     ...
;             XB_SPIN(xb_ld(&bar[XB_XGEN(b.x)]) == gen, bar);
.LBB0_1847:
	global_load_dword v3, v1, s[16:17] sc1
	s_add_i32 s3, s3, 1
	s_mov_b64 s[24:25], -1
	s_waitcnt vmcnt(0)
	v_cmp_ge_u32_e32 vcc, v3, v2
	s_orn2_b64 s[22:23], vcc, exec
	s_branch .LBB0_1844

; __device__ __forceinline__ unsigned xb_ld(unsigned* p)              { return __hip_atomic_load(p, __ATOMIC_RELAXED, __HIP_MEMORY_SCOPE_AGENT); }
; __device__ __forceinline__ unsigned xb_add(unsigned* p, unsigned v) { return __hip_atomic_fetch_add(p, v, __ATOMIC_RELAXED, __HIP_MEMORY_SCOPE_AGENT); }
; #define XB_SPIN(cond, bar) do { unsigned _sp = 0; while (cond) { __builtin_amdgcn_s_sleep(1); \
;     if ((++_sp & 255u) == 0u) { if (xb_ld(&(bar)[XB_TMO])) break; if (_sp > XB_SPIN_CAP) { atomicAdd(&(bar)[XB_TMO], 1u); break; } } } } while (0)
; __device__ __forceinline__ void xcd_barrier(const XcdBarrier& b) {
;     ...
;             asm volatile("buffer_inv sc1" ::: "memory");
;             __builtin_amdgcn_fence(__ATOMIC_RELEASE, "agent");
;             asm volatile("s_waitcnt vmcnt(0)" ::: "memory");
;             const unsigned og = xb_add(&bar[XB_TOP], 1u);
;             const unsigned tg = og / nx;
;             if (og + 1u == (tg + 1u) * nx) xb_add(&bar[XB_TOPGEN], 1u);
;             else XB_SPIN(xb_ld(&bar[XB_TOPGEN]) == tg, bar);
;             asm volatile("" ::: "memory");
;             xb_add(&bar[XB_XGEN(b.x)], 1u);
;             asm volatile("" ::: "memory");
.LBB0_1858:
	s_or_b64 exec, exec, s[12:13]
	v_cvt_f32_u32_e32 v4, v1
	s_waitcnt vmcnt(0)
	v_readfirstlane_b32 s3, v3
	s_add_u32 s12, s82, 0x7500
	s_addc_u32 s13, s83, 0
	v_rcp_iflag_f32_e32 v4, v4
	v_add_u32_e32 v2, s3, v2
	v_add_u32_e32 v5, 1, v2
	s_mov_b64 s[14:15], -1
	v_mul_f32_e32 v3, 0x4f7ffffe, v4
	v_cvt_u32_f32_e32 v3, v3
	v_sub_u32_e32 v4, 0, v1
	v_mul_lo_u32 v4, v4, v3
	v_mul_hi_u32 v4, v3, v4
	v_add_u32_e32 v3, v3, v4
	v_mul_hi_u32 v3, v2, v3
	v_mul_lo_u32 v4, v3, v1
	v_sub_u32_e32 v2, v2, v4
	v_add_u32_e32 v6, 1, v3
	v_cmp_ge_u32_e32 vcc, v2, v1
	v_sub_u32_e32 v4, v2, v1
	s_nop 0
	v_cndmask_b32_e32 v3, v3, v6, vcc
	v_cndmask_b32_e32 v2, v2, v4, vcc
	v_add_u32_e32 v4, 1, v3
	v_cmp_ge_u32_e32 vcc, v2, v1
	s_nop 1
	v_cndmask_b32_e32 v4, v3, v4, vcc
	v_mul_lo_u32 v2, v1, v4
	v_add_u32_e32 v1, v2, v1
	v_cmp_ne_u32_e32 vcc, v5, v1
	v_mov_b64_e32 v[2:3], s[12:13]
	s_and_saveexec_b64 s[10:11], vcc
	s_cbranch_execz .LBB0_1870
	s_add_u32 s12, s8, 0x2400
	s_addc_u32 s13, s9, 0
	v_mov_b32_e32 v4, s98
	v_lshl_add_u32 v4, v4, 1, 1
	v_mov_b32_e32 v1, 0
	global_load_dword v2, v1, s[12:13] sc1
	s_mov_b64 s[18:19], 0
	s_waitcnt vmcnt(0)
	v_cmp_lt_u32_e32 vcc, v2, v4
	s_and_saveexec_b64 s[16:17], vcc
	s_cbranch_execz .LBB0_1869
	s_add_u32 s14, s82, 0x4200
	s_addc_u32 s15, s83, 0
	s_mov_b32 s3, 1
	s_branch .LBB0_1862

; __device__ __forceinline__ unsigned xb_ld(unsigned* p)              { return __hip_atomic_load(p, __ATOMIC_RELAXED, __HIP_MEMORY_SCOPE_AGENT); }
; #define XB_SPIN(cond, bar) do { unsigned _sp = 0; while (cond) { __builtin_amdgcn_s_sleep(1); \
;     if ((++_sp & 255u) == 0u) { if (xb_ld(&(bar)[XB_TMO])) break; if (_sp > XB_SPIN_CAP) { atomicAdd(&(bar)[XB_TMO], 1u); break; } } } } while (0)
; __device__ __forceinline__ void xcd_barrier(const XcdBarrier& b) {
;     ...
;             else XB_SPIN(xb_ld(&bar[XB_TOPGEN]) == tg, bar);
.LBB0_1864:
	global_load_dword v2, v1, s[12:13] sc1
	s_add_i32 s3, s3, 1
	s_mov_b64 s[22:23], -1
	s_waitcnt vmcnt(0)
	v_cmp_ge_u32_e32 vcc, v2, v4
	s_orn2_b64 s[26:27], vcc, exec
	s_branch .LBB0_1861

; #define LAS __attribute__((address_space(3)))
; __global__ void __launch_bounds__(512, 2) dit_fwd(Args args) {
;     extern __shared__ __attribute__((aligned(16))) unsigned char lds_raw[];
;     LAS unsigned char* lds = (LAS unsigned char*)lds_raw;
;     const int tid = threadIdx.x, lane = tid & 63, wave = __builtin_amdgcn_readfirstlane(tid >> 6);
;     const int G = gridDim.x, bid = blockIdx.x;
;     const int gw = bid * 8 + wave, NGW = G * 8;
	.amdhsa_kernel _Z7dit_fwd4Args
		.amdhsa_group_segment_fixed_size 0
		.amdhsa_private_segment_fixed_size 0
		.amdhsa_kernarg_size 440
		.amdhsa_user_sgpr_count 2
		.amdhsa_user_sgpr_dispatch_ptr 0
		.amdhsa_user_sgpr_queue_ptr 0
		.amdhsa_user_sgpr_kernarg_segment_ptr 1
		.amdhsa_user_sgpr_dispatch_id 0
		.amdhsa_user_sgpr_kernarg_preload_length 0
		.amdhsa_user_sgpr_kernarg_preload_offset 0
		.amdhsa_user_sgpr_private_segment_size 0
		.amdhsa_uses_dynamic_stack 0
		.amdhsa_enable_private_segment 0
		.amdhsa_system_sgpr_workgroup_id_x 1
		.amdhsa_system_sgpr_workgroup_id_y 0
		.amdhsa_system_sgpr_workgroup_id_z 0
		.amdhsa_system_sgpr_workgroup_info 0
		.amdhsa_system_vgpr_workitem_id 0
		.amdhsa_next_free_vgpr 252
		.amdhsa_next_free_sgpr 99
		.amdhsa_accum_offset 252
		.amdhsa_reserve_vcc 1
		.amdhsa_float_round_mode_32 0
		.amdhsa_float_round_mode_16_64 0
		.amdhsa_float_denorm_mode_32 3
		.amdhsa_float_denorm_mode_16_64 3
		.amdhsa_dx10_clamp 1
		.amdhsa_ieee_mode 1
		.amdhsa_fp16_overflow 0
		.amdhsa_tg_split 0
		.amdhsa_exception_fp_ieee_invalid_op 0
		.amdhsa_exception_fp_denorm_src 0
		.amdhsa_exception_fp_ieee_div_zero 0
		.amdhsa_exception_fp_ieee_overflow 0
		.amdhsa_exception_fp_ieee_underflow 0
		.amdhsa_exception_fp_ieee_inexact 0
		.amdhsa_exception_int_div_zero 0
	.end_amdhsa_kernel

; #define LAS __attribute__((address_space(3)))
; __global__ void __launch_bounds__(512, 2) dit_fwd(Args args) {
;     extern __shared__ __attribute__((aligned(16))) unsigned char lds_raw[];
;     LAS unsigned char* lds = (LAS unsigned char*)lds_raw;
;     const int tid = threadIdx.x, lane = tid & 63, wave = __builtin_amdgcn_readfirstlane(tid >> 6);
;     const int G = gridDim.x, bid = blockIdx.x;
;     const int gw = bid * 8 + wave, NGW = G * 8;
amdhsa.kernels:
  - .agpr_count:     0
    .args:
      - .offset:         0
        .size:           184
        .value_kind:     by_value
      - .offset:         184
        .size:           4
        .value_kind:     hidden_block_count_x
      - .offset:         188
        .size:           4
        .value_kind:     hidden_block_count_y
      - .offset:         192
        .size:           4
        .value_kind:     hidden_block_count_z
      - .offset:         196
        .size:           2
        .value_kind:     hidden_group_size_x
      - .offset:         198
        .size:           2
        .value_kind:     hidden_group_size_y
      - .offset:         200
        .size:           2
        .value_kind:     hidden_group_size_z
      - .offset:         202
        .size:           2
        .value_kind:     hidden_remainder_x
      - .offset:         204
        .size:           2
        .value_kind:     hidden_remainder_y
      - .offset:         206
        .size:           2
        .value_kind:     hidden_remainder_z
      - .offset:         224
        .size:           8
        .value_kind:     hidden_global_offset_x
      - .offset:         232
        .size:           8
        .value_kind:     hidden_global_offset_y
      - .offset:         240
        .size:           8
        .value_kind:     hidden_global_offset_z
      - .offset:         248
        .size:           2
        .value_kind:     hidden_grid_dims
      - .offset:         304
        .size:           4
        .value_kind:     hidden_dynamic_lds_size
    .group_segment_fixed_size: 0
    .kernarg_segment_align: 8
    .kernarg_segment_size: 440
    .language:       OpenCL C
    .language_version:
      - 2
      - 0
    .max_flat_workgroup_size: 512
    .name:           _Z7dit_fwd4Args
    .private_segment_fixed_size: 0
    .sgpr_count:     105
    .sgpr_spill_count: 107
    .symbol:         _Z7dit_fwd4Args.kd
    .uniform_work_group_size: 1
    .uses_dynamic_stack: false
    .vgpr_count:     252
    .vgpr_spill_count: 0
    .wavefront_size: 64
